# adds: GLA intra-chunk output stage - the 16 V^T fragment loads of both row blocks and the 4 k^T v fragment loads issued as one batch into free VGPRs with counted waits (was ~7 serial round trips)
# baseline (speedup 1.0000x reference)
.LBB0_287:
	s_or_b64 exec, exec, s[14:15]
	s_waitcnt lgkmcnt(0)
	s_barrier
	v_readlane_b32 s11, v254, 45
	ds_read_b128 v[6:9], v129
	s_add_u32 s14, s11, s19
	v_readlane_b32 s11, v254, 46
	s_addc_u32 s15, s11, 0
	v_lshl_add_u64 v[2:3], s[14:15], 0, v[2:3]
	v_lshl_add_u64 v[2:3], v[2:3], 0, v[34:35]
	s_waitcnt lgkmcnt(0)
	global_store_dwordx4 v[2:3], v[6:9], off
	ds_read_b128 v[6:9], v130
	v_lshl_add_u64 v[2:3], s[14:15], 0, v[4:5]
	v_lshl_add_u64 v[2:3], v[2:3], 0, v[34:35]
	v_add_u32_e32 v63, v131, v133
	v_readlane_b32 s14, v255, 4
	s_waitcnt lgkmcnt(0)
	global_store_dwordx4 v[2:3], v[6:9], off
	ds_read_b128 v[2:5], v63 offset:17408
	ds_read_b128 v[18:21], v63 offset:17440
	ds_read_b128 v[22:25], v132
	ds_read_b128 v[26:29], v132 offset:32
	s_waitcnt lgkmcnt(1)
	v_mfma_f32_32x32x16_bf16 v[2:17], v[2:5], v[22:25], 0
	v_readlane_b32 s15, v255, 5
	s_lshl_b32 s11, s18, 8
	s_lshl_b32 s8, s8, 1
	s_waitcnt lgkmcnt(0)
	v_mfma_f32_32x32x16_bf16 v[2:17], v[18:21], v[26:29], v[2:17]
	ds_read_b128 v[18:21], v63 offset:17472
	ds_read_b128 v[30:33], v132 offset:64
	s_waitcnt lgkmcnt(0)
	v_mfma_f32_32x32x16_bf16 v[2:17], v[18:21], v[30:33], v[2:17]
	ds_read_b128 v[18:21], v63 offset:17504
	ds_read_b128 v[66:69], v132 offset:96
	s_waitcnt lgkmcnt(0)
	v_mfma_f32_32x32x16_bf16 v[2:17], v[18:21], v[66:69], v[2:17]
	ds_read_b128 v[18:21], v63 offset:17536
	ds_read_b128 v[150:153], v132 offset:128
	s_waitcnt lgkmcnt(0)
	v_mfma_f32_32x32x16_bf16 v[2:17], v[18:21], v[150:153], v[2:17]
	ds_read_b128 v[18:21], v63 offset:17568
	ds_read_b128 v[154:157], v132 offset:160
	s_waitcnt lgkmcnt(0)
	v_mfma_f32_32x32x16_bf16 v[2:17], v[18:21], v[154:157], v[2:17]
	ds_read_b128 v[18:21], v63 offset:17600
	ds_read_b128 v[158:161], v132 offset:192
	s_waitcnt lgkmcnt(0)
	v_mfma_f32_32x32x16_bf16 v[2:17], v[18:21], v[158:161], v[2:17]
	ds_read_b128 v[18:21], v63 offset:17632
	ds_read_b128 v[162:165], v132 offset:224
	s_waitcnt lgkmcnt(0)
	v_mfma_f32_32x32x16_bf16 v[2:17], v[18:21], v[162:165], v[2:17]
	s_nop 11
	v_cndmask_b32_e64 v18, v2, 0, s[14:15]
	v_readlane_b32 s14, v255, 6
	v_readlane_b32 s15, v255, 7
	v_cndmask_b32_e64 v149, v18, v2, s[12:13]
	v_cndmask_b32_e64 v168, 0, v3, s[12:13]
	v_cndmask_b32_e64 v169, v4, 0, s[14:15]
	v_readlane_b32 s14, v255, 8
	v_readlane_b32 s15, v255, 9
	ds_read_b128 v[18:21], v63 offset:26144
	v_cndmask_b32_e64 v172, v7, 0, s[20:21]
	v_cndmask_b32_e64 v170, v5, 0, s[14:15]
	ds_read_b128 v[2:5], v63 offset:26112
	v_readlane_b32 s14, v255, 10
	v_readlane_b32 s15, v255, 11
	v_cndmask_b32_e64 v173, v8, 0, s[22:23]
	v_cndmask_b32_e64 v174, v9, 0, s[24:25]
	v_cndmask_b32_e64 v171, v6, 0, s[14:15]
	v_cndmask_b32_e64 v175, v10, 0, s[26:27]
	v_cndmask_b32_e64 v176, v11, 0, s[28:29]
	v_cndmask_b32_e64 v177, v12, 0, s[30:31]
	v_cndmask_b32_e64 v178, v13, 0, s[34:35]
	v_cndmask_b32_e64 v179, v14, 0, s[2:3]
	v_cndmask_b32_e64 v180, v15, 0, s[38:39]
	v_cndmask_b32_e64 v181, v16, 0, s[40:41]
	v_cndmask_b32_e64 v182, v17, 0, s[42:43]
	s_waitcnt lgkmcnt(0)
	v_mfma_f32_32x32x16_bf16 v[2:17], v[2:5], v[22:25], 0
	v_readlane_b32 s14, v254, 49
	v_cvt_pk_bf16_f32 v22, v175, v176
	v_cvt_pk_bf16_f32 v23, v177, v178
	v_cvt_pk_bf16_f32 v24, v179, v180
	v_cvt_pk_bf16_f32 v25, v181, v182
	v_mfma_f32_32x32x16_bf16 v[2:17], v[18:21], v[26:29], v[2:17]
	ds_read_b128 v[18:21], v63 offset:26176
	s_waitcnt lgkmcnt(0)
	v_mfma_f32_32x32x16_bf16 v[2:17], v[18:21], v[30:33], v[2:17]
	ds_read_b128 v[18:21], v63 offset:26208
	s_waitcnt lgkmcnt(0)
	v_mfma_f32_32x32x16_bf16 v[2:17], v[18:21], v[66:69], v[2:17]
	ds_read_b128 v[18:21], v63 offset:26240
	v_lshl_add_u64 v[68:69], v[40:41], 0, s[8:9]
	v_lshlrev_b64 v[66:67], 15, v[64:65]
	v_lshl_add_u64 v[66:67], v[58:59], 0, v[66:67]
	v_lshlrev_b64 v[64:65], 16, v[64:65]
	s_waitcnt lgkmcnt(0)
	v_mfma_f32_32x32x16_bf16 v[2:17], v[18:21], v[150:153], v[2:17]
	ds_read_b128 v[18:21], v63 offset:26272
	s_waitcnt lgkmcnt(0)
	v_mfma_f32_32x32x16_bf16 v[2:17], v[18:21], v[154:157], v[2:17]
	ds_read_b128 v[18:21], v63 offset:26304
	s_waitcnt lgkmcnt(0)
	v_mfma_f32_32x32x16_bf16 v[2:17], v[18:21], v[158:161], v[2:17]
	ds_read_b128 v[18:21], v63 offset:26336
	s_waitcnt lgkmcnt(0)
	v_mfma_f32_32x32x16_bf16 v[2:17], v[18:21], v[162:165], v[2:17]
	v_or_b32_e32 v163, s11, v167
	v_cvt_pk_bf16_f32 v19, v169, v170
	v_cvt_pk_bf16_f32 v20, v171, v172
	v_cvt_pk_bf16_f32 v21, v173, v174
	s_nop 7
	v_cndmask_b32_e64 v18, v2, 0, s[44:45]
	v_cndmask_b32_e64 v30, v18, v2, s[46:47]
	v_add_u32_e32 v2, s14, v163
	v_cndmask_b32_e64 v31, 0, v3, s[46:47]
	v_ashrrev_i32_e32 v3, 31, v2
	v_lshlrev_b64 v[2:3], 12, v[2:3]
	v_lshl_add_u64 v[152:153], v[68:69], 0, v[2:3]
	v_cndmask_b32_e64 v32, v4, 0, s[50:51]
	v_cndmask_b32_e64 v33, v5, 0, s[52:53]
	global_load_dwordx2 v[2:3], v[152:153], off
	global_load_dwordx2 v[4:5], v[152:153], off offset:16
	global_load_dwordx2 v[26:27], v[152:153], off offset:32
	global_load_dwordx2 v[28:29], v[152:153], off offset:48
	global_load_dwordx2 v[198:199], v[152:153], off offset:64
	global_load_dwordx2 v[200:201], v[152:153], off offset:80
	global_load_dwordx2 v[202:203], v[152:153], off offset:96
	global_load_dwordx2 v[204:205], v[152:153], off offset:112
	v_readlane_b32 s14, v254, 51
	s_nop 1
	v_add_u32_e32 v212, s14, v163
	v_ashrrev_i32_e32 v213, 31, v212
	v_lshlrev_b64 v[212:213], 12, v[212:213]
	v_lshl_add_u64 v[230:231], v[68:69], 0, v[212:213]
	global_load_dwordx2 v[206:207], v[230:231], off
	global_load_dwordx2 v[208:209], v[230:231], off offset:16
	global_load_dwordx2 v[218:219], v[230:231], off offset:32
	global_load_dwordx2 v[220:221], v[230:231], off offset:48
	global_load_dwordx2 v[222:223], v[230:231], off offset:64
	global_load_dwordx2 v[224:225], v[230:231], off offset:80
	global_load_dwordx2 v[226:227], v[230:231], off offset:96
	global_load_dwordx2 v[228:229], v[230:231], off offset:112
	v_add_u32_e32 v212, s11, v134
	v_ashrrev_i32_e32 v213, 31, v212
	v_lshlrev_b64 v[212:213], 12, v[212:213]
	v_lshl_add_u64 v[232:233], s[6:7], 0, v[212:213]
	v_lshl_add_u64 v[232:233], v[232:233], 0, s[8:9]
	v_mov_b32_e32 v234, v62
	v_mov_b32_e32 v235, v35
	v_lshl_add_u64 v[232:233], v[232:233], 0, v[234:235]
	global_load_dwordx4 v[238:241], v[232:233], off
	global_load_dwordx4 v[242:245], v[232:233], off offset:32
	global_load_dwordx4 v[246:249], v[232:233], off offset:64
	global_load_dwordx4 v[250:253], v[232:233], off offset:96
	v_cvt_pk_bf16_f32 v18, v149, v168
	v_cndmask_b32_e64 v63, v6, 0, s[54:55]
	v_cndmask_b32_e64 v150, v7, 0, s[78:79]
	v_cndmask_b32_e64 v151, v8, 0, s[96:97]
	v_cndmask_b32_e64 v154, v9, 0, s[0:1]
	v_cndmask_b32_e64 v155, v10, 0, s[76:77]
	v_cndmask_b32_e64 v156, v11, 0, s[4:5]
	v_cndmask_b32_e64 v157, v12, 0, s[64:65]
	v_cndmask_b32_e64 v158, v13, 0, s[66:67]
	v_cndmask_b32_e64 v159, v14, 0, s[68:69]
	v_cndmask_b32_e64 v160, v15, 0, s[70:71]
	v_cndmask_b32_e64 v161, v16, 0, s[72:73]
	v_cndmask_b32_e64 v162, v17, 0, s[74:75]
	s_waitcnt vmcnt(18)
	v_mfma_f32_32x32x16_bf16 v[2:17], v[2:5], v[18:21], 0
	s_waitcnt vmcnt(16)
	v_mfma_f32_32x32x16_bf16 v[2:17], v[26:29], v[22:25], v[2:17]
	v_cvt_pk_bf16_f32 v26, v30, v31
	v_cvt_pk_bf16_f32 v27, v32, v33
	v_cvt_pk_bf16_f32 v28, v63, v150
	v_cvt_pk_bf16_f32 v29, v151, v154
	v_mov_b32_e32 v63, v35
	s_waitcnt vmcnt(14)
	v_mfma_f32_32x32x16_bf16 v[2:17], v[198:201], v[26:29], v[2:17]
	v_cvt_pk_bf16_f32 v30, v155, v156
	v_cvt_pk_bf16_f32 v31, v157, v158
	v_cvt_pk_bf16_f32 v32, v159, v160
	v_cvt_pk_bf16_f32 v33, v161, v162
	s_waitcnt vmcnt(12)
	s_nop 0
	v_mfma_f32_32x32x16_bf16 v[2:17], v[202:205], v[30:33], v[2:17]
	s_nop 11
	v_cvt_pk_bf16_f32 v2, v2, v3
	v_cvt_pk_bf16_f32 v3, v4, v5
	v_cvt_pk_bf16_f32 v4, v6, v7
	v_cvt_pk_bf16_f32 v5, v8, v9
	global_store_dwordx4 v[66:67], v[2:5], off
	s_nop 1
	v_cvt_pk_bf16_f32 v2, v10, v11
	v_cvt_pk_bf16_f32 v3, v12, v13
	v_cvt_pk_bf16_f32 v4, v14, v15
	v_cvt_pk_bf16_f32 v5, v16, v17
	global_store_dwordx4 v[66:67], v[2:5], off offset:1024
	s_nop 1
	s_waitcnt vmcnt(12)
	v_mfma_f32_32x32x16_bf16 v[2:17], v[206:209], v[18:21], 0
	s_waitcnt vmcnt(10)
	v_mfma_f32_32x32x16_bf16 v[2:17], v[218:221], v[22:25], v[2:17]
	s_waitcnt vmcnt(8)
	v_mfma_f32_32x32x16_bf16 v[2:17], v[222:225], v[26:29], v[2:17]
	s_waitcnt vmcnt(6)
	v_mfma_f32_32x32x16_bf16 v[2:17], v[226:229], v[30:33], v[2:17]
	s_nop 11
	v_cvt_pk_bf16_f32 v2, v2, v3
	v_cvt_pk_bf16_f32 v3, v4, v5
	v_cvt_pk_bf16_f32 v4, v6, v7
	v_cvt_pk_bf16_f32 v5, v8, v9
	global_store_dwordx4 v[66:67], v[2:5], off offset:2048
	s_nop 1
	v_cvt_pk_bf16_f32 v2, v10, v11
	v_cvt_pk_bf16_f32 v3, v12, v13
	v_cvt_pk_bf16_f32 v4, v14, v15
	v_cvt_pk_bf16_f32 v5, v16, v17
	global_store_dwordx4 v[66:67], v[2:5], off offset:3072
	s_nop 1
	v_add_u32_e32 v63, v131, v137
	ds_read_b128 v[2:5], v63 offset:34816
	ds_read_b128 v[66:69], v63 offset:34848
	v_readlane_b32 s8, v254, 53
	s_waitcnt vmcnt(7) lgkmcnt(1)
	v_mfma_f32_32x32x16_bf16 v[2:17], v[238:241], v[2:5], 0
	s_waitcnt vmcnt(6) lgkmcnt(0)
	v_mfma_f32_32x32x16_bf16 v[2:17], v[242:245], v[66:69], v[2:17]
	ds_read_b128 v[66:69], v63 offset:34880
	s_waitcnt vmcnt(5) lgkmcnt(0)
	v_mfma_f32_32x32x16_bf16 v[2:17], v[246:249], v[66:69], v[2:17]
	ds_read_b128 v[66:69], v63 offset:34912
	s_waitcnt vmcnt(4) lgkmcnt(0)
	v_mfma_f32_32x32x16_bf16 v[2:17], v[250:253], v[66:69], v[2:17]
	v_add_u32_e32 v66, s8, v135
	v_readlane_b32 s8, v254, 54
	s_nop 1
	v_add_u32_e32 v67, s8, v135
	v_readlane_b32 s8, v254, 55
	s_nop 5
	v_cvt_pk_bf16_f32 v2, v2, s0
	ds_write_b16 v136, v2 offset:59392
	v_cvt_pk_bf16_f32 v2, v3, s0
	ds_write_b16 v136, v2 offset:59648
	v_cvt_pk_bf16_f32 v2, v4, s0
	ds_write_b16 v136, v2 offset:59904
	v_cvt_pk_bf16_f32 v2, v5, s0
	ds_write_b16 v136, v2 offset:60160
	v_cvt_pk_bf16_f32 v2, v6, s0
	ds_write_b16 v136, v2 offset:61440
	v_cvt_pk_bf16_f32 v2, v7, s0
	ds_write_b16 v136, v2 offset:61696
	v_cvt_pk_bf16_f32 v2, v8, s0
	ds_write_b16 v136, v2 offset:61952
	v_cvt_pk_bf16_f32 v2, v9, s0
	ds_write_b16 v136, v2 offset:62208
	v_cvt_pk_bf16_f32 v2, v10, s0
	ds_write_b16 v136, v2 offset:63488
	v_cvt_pk_bf16_f32 v2, v11, s0
	ds_write_b16 v136, v2 offset:63744
	v_cvt_pk_bf16_f32 v2, v12, s0
	ds_write_b16 v136, v2 offset:64000
	v_cvt_pk_bf16_f32 v2, v13, s0
	ds_write_b16 v136, v2 offset:64256
	v_cvt_pk_bf16_f32 v2, v14, s0
	ds_write_b16 v66, v2 offset:59392
	v_cvt_pk_bf16_f32 v2, v15, s0
	ds_write_b16 v67, v2 offset:59392
	v_cvt_pk_bf16_f32 v2, v16, s0
	v_add_u32_e32 v68, s8, v135
	v_readlane_b32 s8, v254, 57
	ds_write_b16 v68, v2 offset:59392
	v_cvt_pk_bf16_f32 v2, v17, s0
	v_add_u32_e32 v69, s8, v135
	ds_write_b16 v69, v2 offset:59392
	ds_read_b128 v[2:5], v63 offset:39424
	ds_read_b128 v[150:153], v63 offset:39456
	s_waitcnt lgkmcnt(1)
	v_mfma_f32_32x32x16_bf16 v[2:17], v[238:241], v[2:5], 0
	v_readlane_b32 s8, v254, 36
	s_add_i32 s10, s10, s8
	v_readlane_b32 s8, v255, 12
	s_add_i32 s16, s16, s8
	v_readlane_b32 s8, v255, 13
	s_add_i32 s17, s17, s8
	s_cmpk_gt_i32 s10, 0x1ff
	s_waitcnt lgkmcnt(0)
	v_mfma_f32_32x32x16_bf16 v[2:17], v[242:245], v[150:153], v[2:17]
	ds_read_b128 v[150:153], v63 offset:39488
	s_waitcnt lgkmcnt(0)
	v_mfma_f32_32x32x16_bf16 v[2:17], v[246:249], v[150:153], v[2:17]
	ds_read_b128 v[150:153], v63 offset:39520
	s_waitcnt lgkmcnt(0)
	v_mfma_f32_32x32x16_bf16 v[2:17], v[250:253], v[150:153], v[2:17]
	s_nop 11
	v_cvt_pk_bf16_f32 v2, v2, s0
	ds_write_b16 v136, v2 offset:59456
	v_cvt_pk_bf16_f32 v2, v3, s0
	ds_write_b16 v136, v2 offset:59712
	v_cvt_pk_bf16_f32 v2, v4, s0
	ds_write_b16 v136, v2 offset:59968
	v_cvt_pk_bf16_f32 v2, v5, s0
	ds_write_b16 v136, v2 offset:60224
	v_cvt_pk_bf16_f32 v2, v6, s0
	ds_write_b16 v136, v2 offset:61504
	v_cvt_pk_bf16_f32 v2, v7, s0
	ds_write_b16 v136, v2 offset:61760
	v_cvt_pk_bf16_f32 v2, v8, s0
	ds_write_b16 v136, v2 offset:62016
	v_cvt_pk_bf16_f32 v2, v9, s0
	ds_write_b16 v136, v2 offset:62272
	v_cvt_pk_bf16_f32 v2, v10, s0
	ds_write_b16 v136, v2 offset:63552
	v_cvt_pk_bf16_f32 v2, v11, s0
	ds_write_b16 v136, v2 offset:63808
	v_cvt_pk_bf16_f32 v2, v12, s0
	ds_write_b16 v136, v2 offset:64064
	v_cvt_pk_bf16_f32 v2, v13, s0
	ds_write_b16 v136, v2 offset:64320
	v_cvt_pk_bf16_f32 v2, v14, s0
	ds_write_b16 v66, v2 offset:59456
	v_cvt_pk_bf16_f32 v2, v15, s0
	ds_write_b16 v67, v2 offset:59456
	v_cvt_pk_bf16_f32 v2, v16, s0
	ds_write_b16 v68, v2 offset:59456
	v_cvt_pk_bf16_f32 v2, v17, s0
	ds_write_b16 v69, v2 offset:59456
	ds_read_b128 v[2:5], v63 offset:44032
	ds_read_b128 v[150:153], v63 offset:44064
	s_waitcnt lgkmcnt(1)
	v_mfma_f32_32x32x16_bf16 v[2:17], v[238:241], v[2:5], 0
	s_waitcnt lgkmcnt(0)
	v_mfma_f32_32x32x16_bf16 v[2:17], v[242:245], v[150:153], v[2:17]
	ds_read_b128 v[150:153], v63 offset:44096
	s_waitcnt lgkmcnt(0)
	v_mfma_f32_32x32x16_bf16 v[2:17], v[246:249], v[150:153], v[2:17]
	ds_read_b128 v[150:153], v63 offset:44128
	s_waitcnt lgkmcnt(0)
	v_mfma_f32_32x32x16_bf16 v[2:17], v[250:253], v[150:153], v[2:17]
	s_nop 11
	v_cvt_pk_bf16_f32 v2, v2, s0
	ds_write_b16 v136, v2 offset:59520
	v_cvt_pk_bf16_f32 v2, v3, s0
	ds_write_b16 v136, v2 offset:59776
	v_cvt_pk_bf16_f32 v2, v4, s0
	ds_write_b16 v136, v2 offset:60032
	v_cvt_pk_bf16_f32 v2, v5, s0
	ds_write_b16 v136, v2 offset:60288
	v_cvt_pk_bf16_f32 v2, v6, s0
	ds_write_b16 v136, v2 offset:61568
	v_cvt_pk_bf16_f32 v2, v7, s0
	ds_write_b16 v136, v2 offset:61824
	v_cvt_pk_bf16_f32 v2, v8, s0
	ds_write_b16 v136, v2 offset:62080
	v_cvt_pk_bf16_f32 v2, v9, s0
	ds_write_b16 v136, v2 offset:62336
	v_cvt_pk_bf16_f32 v2, v10, s0
	ds_write_b16 v136, v2 offset:63616
	v_cvt_pk_bf16_f32 v2, v11, s0
	ds_write_b16 v136, v2 offset:63872
	v_cvt_pk_bf16_f32 v2, v12, s0
	ds_write_b16 v136, v2 offset:64128
	v_cvt_pk_bf16_f32 v2, v13, s0
	ds_write_b16 v136, v2 offset:64384
	v_cvt_pk_bf16_f32 v2, v14, s0
	ds_write_b16 v66, v2 offset:59520
	v_cvt_pk_bf16_f32 v2, v15, s0
	ds_write_b16 v67, v2 offset:59520
	v_cvt_pk_bf16_f32 v2, v16, s0
	ds_write_b16 v68, v2 offset:59520
	v_cvt_pk_bf16_f32 v2, v17, s0
	ds_write_b16 v69, v2 offset:59520
	ds_read_b128 v[2:5], v63 offset:48640
	ds_read_b128 v[150:153], v63 offset:48672
	s_waitcnt lgkmcnt(1)
	v_mfma_f32_32x32x16_bf16 v[2:17], v[238:241], v[2:5], 0
	ds_read_b128 v[26:29], v63 offset:48704
	s_waitcnt lgkmcnt(1)
	v_mfma_f32_32x32x16_bf16 v[2:17], v[242:245], v[150:153], v[2:17]
	s_waitcnt lgkmcnt(0)
	v_mfma_f32_32x32x16_bf16 v[2:17], v[246:249], v[26:29], v[2:17]
	ds_read_b128 v[22:25], v63 offset:48736
	s_waitcnt lgkmcnt(0)
	v_mfma_f32_32x32x16_bf16 v[2:17], v[250:253], v[22:25], v[2:17]
	s_nop 11
	v_cvt_pk_bf16_f32 v2, v2, s0
	ds_write_b16 v136, v2 offset:59584
	v_cvt_pk_bf16_f32 v2, v3, s0
	ds_write_b16 v136, v2 offset:59840
	v_cvt_pk_bf16_f32 v2, v4, s0
	ds_write_b16 v136, v2 offset:60096
	v_cvt_pk_bf16_f32 v2, v5, s0
	ds_write_b16 v136, v2 offset:60352
	v_cvt_pk_bf16_f32 v2, v6, s0
	ds_write_b16 v136, v2 offset:61632
	v_cvt_pk_bf16_f32 v2, v7, s0
	ds_write_b16 v136, v2 offset:61888
	v_cvt_pk_bf16_f32 v2, v8, s0
	ds_write_b16 v136, v2 offset:62144
	v_cvt_pk_bf16_f32 v2, v9, s0
	ds_write_b16 v136, v2 offset:62400
	v_cvt_pk_bf16_f32 v2, v10, s0
	ds_write_b16 v136, v2 offset:63680
	v_cvt_pk_bf16_f32 v2, v11, s0
	ds_write_b16 v136, v2 offset:63936
	v_cvt_pk_bf16_f32 v2, v12, s0
	ds_write_b16 v136, v2 offset:64192
	v_cvt_pk_bf16_f32 v2, v13, s0
	ds_write_b16 v136, v2 offset:64448
	v_cvt_pk_bf16_f32 v2, v14, s0
	ds_write_b16 v66, v2 offset:59584
	v_cvt_pk_bf16_f32 v2, v15, s0
	ds_write_b16 v67, v2 offset:59584
	v_cvt_pk_bf16_f32 v2, v16, s0
	ds_write_b16 v68, v2 offset:59584
	v_cvt_pk_bf16_f32 v2, v17, s0
	ds_write_b16 v69, v2 offset:59584
	s_waitcnt lgkmcnt(0)
	v_add_u32_e32 v4, v70, v138
	ds_read_b128 v[4:7], v4 offset:59392
	v_lshl_add_u64 v[2:3], v[38:39], 0, v[64:65]
	v_lshl_add_u64 v[8:9], v[2:3], 0, v[42:43]
	s_waitcnt lgkmcnt(0)
	global_store_dwordx4 v[8:9], v[4:7], off
	s_nop 1
	v_add_u32_e32 v4, v70, v139
	ds_read_b128 v[4:7], v4 offset:59392
	v_lshl_add_u64 v[8:9], v[2:3], 0, v[44:45]
	s_waitcnt lgkmcnt(0)
	global_store_dwordx4 v[8:9], v[4:7], off
	s_nop 1
	v_add_u32_e32 v4, v70, v140
	ds_read_b128 v[4:7], v4 offset:59392
	v_lshl_add_u64 v[8:9], v[2:3], 0, v[46:47]
	s_waitcnt lgkmcnt(0)
	global_store_dwordx4 v[8:9], v[4:7], off
	s_nop 1
	v_add_u32_e32 v4, v70, v141
	ds_read_b128 v[4:7], v4 offset:59392
	v_lshl_add_u64 v[8:9], v[2:3], 0, v[48:49]
	s_waitcnt lgkmcnt(0)
	global_store_dwordx4 v[8:9], v[4:7], off
	s_nop 1
	v_add_u32_e32 v4, v70, v143
	ds_read_b128 v[4:7], v4 offset:59392
	v_lshl_add_u64 v[8:9], v[2:3], 0, v[50:51]
	s_waitcnt lgkmcnt(0)
	global_store_dwordx4 v[8:9], v[4:7], off
	s_nop 1
	v_add_u32_e32 v4, v70, v144
	ds_read_b128 v[4:7], v4 offset:59392
	v_lshl_add_u64 v[8:9], v[2:3], 0, v[52:53]
	s_waitcnt lgkmcnt(0)
	global_store_dwordx4 v[8:9], v[4:7], off
	s_nop 1
	v_add_u32_e32 v4, v70, v145
	ds_read_b128 v[4:7], v4 offset:59392
	v_lshl_add_u64 v[8:9], v[2:3], 0, v[54:55]
	v_lshl_add_u64 v[2:3], v[2:3], 0, v[56:57]
	s_waitcnt lgkmcnt(0)
	global_store_dwordx4 v[8:9], v[4:7], off
	s_nop 1
	v_add_u32_e32 v4, v70, v146
	ds_read_b128 v[4:7], v4 offset:59392
	s_waitcnt lgkmcnt(0)
	global_store_dwordx4 v[2:3], v[4:7], off
	s_barrier
	s_cbranch_scc1 .LBB0_294
